# v043 + GEMM1 phase prologue: the four row-id loads issued together and waited once
# speedup vs baseline: 1.0062x; 1.0062x over previous
.Lfz_nostag:
	s_load_dwordx2 s[40:41], s[44:45], 0xa0
	s_lshl_b32 s7, s25, 6
	v_lshlrev_b32_e32 v5, 4, v4
	v_and_b32_e32 v6, 32, v4
	v_bfe_u32 v8, v4, 2, 26
	s_waitcnt lgkmcnt(0)
	s_add_u32 s42, s40, 0x33900000
	s_addc_u32 s43, s41, 0
	s_lshl_b32 s4, s52, 27
	s_add_u32 s4, s40, s4
	s_addc_u32 s5, s41, 0
	v_lshrrev_b32_e32 v9, 1, v4
	v_lshrrev_b32_e32 v10, 5, v4
	v_bfe_u32 v11, v5, 6, 2
	s_add_u32 s8, s4, 0x3900000
	v_bitop3_b32 v6, v5, v6, 48 bitop3:0x6c
	v_and_b32_e32 v8, 0x3fffc0, v8
	v_and_b32_e32 v9, 24, v9
	v_and_or_b32 v10, v10, 4, v11
	s_addc_u32 s9, s5, 0
	v_lshrrev_b32_e32 v7, 3, v4
	v_or3_b32 v8, v10, v9, v8
	v_and_or_b32 v9, v4, 64, v6
	v_bfe_u32 v4, v5, 6, 4
	s_mov_b32 s5, 0x1fffff0
	v_and_or_b32 v4, v7, s5, v4
	v_readlane_b32 s5, v254, 37
	s_add_u32 s46, s40, 0x37d00000
	s_addc_u32 s47, s41, 0
	v_add_u32_e32 v4, s5, v4
	v_ashrrev_i32_e32 v5, 31, v4
	v_lshl_add_u64 v[6:7], v[4:5], 2, s[46:47]
	global_load_dword v5, v[6:7], off
	global_load_dword v10, v[6:7], off offset:256
	v_add_u32_e32 v12, 0x80, v4
	v_ashrrev_i32_e32 v13, 31, v12
	v_lshl_add_u64 v[12:13], v[12:13], 2, s[46:47]
	v_add_u32_e32 v14, 0xc0, v4
	v_ashrrev_i32_e32 v15, 31, v14
	v_lshl_add_u64 v[14:15], v[14:15], 2, s[46:47]
	global_load_dword v11, v[12:13], off
	global_load_dword v14, v[14:15], off
	s_lshl_b32 s4, s24, 10
	v_readlane_b32 s12, v254, 40
	v_readlane_b32 s13, v254, 41
	s_add_u32 s74, s8, s12
	v_lshl_or_b32 v194, v8, 10, v9
	s_addc_u32 s75, s9, s13
	s_add_i32 s10, s4, 0
	s_add_i32 s12, s10, 0x10000
	s_mov_b64 s[4:5], s[74:75]
	s_mov_b32 m0, s12
	s_waitcnt vmcnt(0)
	v_lshl_or_b32 v195, v5, 10, v9
	v_lshl_or_b32 v196, v10, 10, v9
	v_lshl_or_b32 v197, v11, 10, v9
	v_lshl_or_b32 v198, v14, 10, v9
	v_mov_b32_e32 v4, v194
	s_nop 0
	global_load_lds_dwordx4 v4, s[4:5]
	s_add_u32 s4, s74, 0x20000
	s_addc_u32 s5, s75, 0
	v_mov_b32_e32 v4, v194
	s_add_i32 s13, s10, 0x12000
	s_mov_b32 m0, s13
	s_add_i32 s14, s10, 0x14000
	global_load_lds_dwordx4 v4, s[4:5]
	s_add_u32 s4, s74, 0x8000
	s_addc_u32 s5, s75, 0
	v_mov_b32_e32 v4, v194
	s_mov_b32 m0, s14
	s_nop 0
	global_load_lds_dwordx4 v4, s[4:5]
	s_add_u32 s4, s74, 0x28000
	s_addc_u32 s5, s75, 0
	v_mov_b32_e32 v4, v194
	s_add_i32 s15, s10, 0x16000
	s_mov_b32 m0, s15
	s_add_i32 s16, s10, 0x2000
	global_load_lds_dwordx4 v4, s[4:5]
	s_mov_b64 s[4:5], s[42:43]
	v_mov_b32_e32 v4, v195
	s_mov_b32 m0, s10
	s_add_i32 s17, s10, 0x4000
	global_load_lds_dwordx4 v4, s[4:5]
	v_mov_b32_e32 v4, v196
	s_mov_b32 m0, s16
	s_add_i32 s26, s10, 0x6000
	global_load_lds_dwordx4 v4, s[4:5]
	s_mov_b64 s[4:5], s[42:43]
	v_mov_b32_e32 v4, v197
	s_mov_b32 m0, s17
	s_cmp_eq_u32 s25, 1
	global_load_lds_dwordx4 v4, s[4:5]
	v_mov_b32_e32 v4, v198
	s_mov_b32 m0, s26
	s_cselect_b64 s[48:49], -1, 0
	global_load_lds_dwordx4 v4, s[4:5]
	s_cmp_lg_u32 s25, 1
	s_cbranch_scc1 .LBB0_1240
	s_barrier
